# v15 with 6 instead of 8 expert weight mats converted per ut_att window
# baseline (speedup 1.0000x reference)
.LBB0_654:
	s_barrier
	v_readlane_b32 s46, v255, 4
	s_sub_i32 s42, s88, 0x80
	s_lshl_b32 s42, s42, 3
	s_lshr_b32 s5, s33, 6
	s_add_i32 s42, s42, s5
	s_mul_i32 s5, s5, 0x4200
	s_movk_i32 s45, 122
	s_movk_i32 s4, 6
	s_movk_i32 vcc_lo, 116
	s_movk_i32 vcc_hi, 6
	s_cmp_eq_u32 s46, 1
	s_cselect_b32 s45, vcc_lo, s45
	s_cselect_b32 s4, vcc_hi, s4
	s_lshl_b32 s44, s4, 9
	s_mul_i32 s43, s4, 0x300
	v_readlane_b32 s8, v252, 0
	v_readlane_b32 s9, v252, 1
	v_mbcnt_lo_u32_b32 v13, -1, 0
	v_mbcnt_hi_u32_b32 v13, -1, v13
	s_load_dwordx2 s[6:7], s[8:9], 0xa0
	s_load_dwordx2 s[10:11], s[8:9], 0xd8
	s_load_dwordx2 s[8:9], s[8:9], 0xb0
	s_movk_i32 s46, 0x84
	s_movk_i32 s47, 0x840
	v_and_b32_e32 v14, 31, v13
	v_lshlrev_b32_e32 v14, 2, v14
	v_lshrrev_b32_e32 v15, 5, v13
	v_mov_b32_e32 v4, s5
	v_mad_u32_u24 v4, v15, s46, v4
	v_add_u32_e32 v4, v4, v14
	v_and_b32_e32 v10, 7, v13
	v_lshrrev_b32_e32 v11, 3, v13
	v_mov_b32_e32 v5, s5
	v_mad_u32_u24 v5, v10, s47, v5
	v_lshl_add_u32 v5, v11, 2, v5
	v_lshlrev_b32_e32 v6, 10, v11
	v_lshl_add_u32 v6, v10, 4, v6
	v_add_u32_e32 v7, 0x2000, v6
	v_add_u32_e32 v8, 0x4000, v6
	v_add_u32_e32 v9, 0x6000, v6
	s_waitcnt lgkmcnt(0)
	s_cmp_lt_u32 s42, s43
	s_cbranch_scc0 .LcvU_done
	s_cmp_lt_u32 s42, s44
	s_cbranch_scc0 .LcvU_dn0
	s_lshr_b32 s4, s42, 9
	s_add_i32 s4, s4, s45
	s_bfe_u32 s5, s42, 0x30006
	s_and_b32 vcc_lo, s42, 63
	s_lshl_b32 s46, s4, 23
	s_lshl_b32 s47, s5, 20
	s_add_u32 s46, s46, s47
	s_lshl_b32 s47, vcc_lo, 7
	s_add_u32 s46, s46, s47
	s_add_u32 s46, s46, s6
	s_addc_u32 s47, s7, 0
	s_lshl_b32 s52, s4, 21
	s_add_u32 s52, s52, 0x4400000
	s_lshl_b32 s53, s5, 7
	s_add_u32 s52, s52, s53
	s_bfe_u32 s53, vcc_lo, 0x30002
	s_lshl_b32 s53, s53, 18
	s_add_u32 s52, s52, s53
	s_lshr_b32 s53, vcc_lo, 5
	s_lshl_b32 s53, s53, 17
	s_add_u32 s52, s52, s53
	s_and_b32 s53, vcc_lo, 3
	s_lshl_b32 s53, s53, 15
	s_add_u32 s52, s52, s53
	s_add_u32 s52, s52, s10
	s_addc_u32 s53, s11, 0
	s_mov_b32 s51, 0x42000000
	s_movk_i32 s5, 0x2000
	s_movk_i32 s4, 0x4000
	s_branch .LcvU_ld0

c_jobs:
	.long	4
	.long	2840
	.long	1024
	.long	0
	.long	1024
	.long	0
	.long	1
	.long	2
	.quad	2908160
	.quad	2097152
	.quad	2097152
	.long	0
	.long	0
	.long	4
	.long	2840
	.long	1024
	.long	1536
	.long	512
	.long	1024
	.long	1
	.long	2
	.quad	2908160
	.quad	2097152
	.quad	2097152
	.long	0
	.long	0
	.long	4
	.long	2840
	.long	1024
	.long	2048
	.long	128
	.long	1536
	.long	1
	.long	2
	.quad	2908160
	.quad	2097152
	.quad	2097152
	.long	0
	.long	0
	.long	4
	.long	2840
	.long	1024
	.long	2176
	.long	128
	.long	1664
	.long	1
	.long	2
	.quad	2908160
	.quad	2097152
	.quad	2097152
	.long	0
	.long	0
	.long	4
	.long	2840
	.long	1024
	.long	2304
	.long	128
	.long	1792
	.long	1
	.long	2
	.quad	2908160
	.quad	2097152
	.quad	2097152
	.long	0
	.long	0
	.long	4
	.long	2840
	.long	1024
	.long	2560
	.long	128
	.long	1920
	.long	1
	.long	2
	.quad	2908160
	.quad	2097152
	.quad	2097152
	.long	0
	.long	0
	.long	4
	.long	2840
	.long	1024
	.long	1024
	.long	512
	.long	0
	.long	0
	.long	2
	.quad	2908160
	.quad	10485760
	.quad	786432
	.long	0
	.long	0
	.long	4
	.long	2840
	.long	1024
	.long	2432
	.long	128
	.long	512
	.long	0
	.long	2
	.quad	2908160
	.quad	10485760
	.quad	786432
	.long	0
	.long	0
	.long	4
	.long	2840
	.long	1024
	.long	2688
	.long	128
	.long	640
	.long	0
	.long	2
	.quad	2908160
	.quad	10485760
	.quad	786432
	.long	0
	.long	0
	.long	5
	.long	1024
	.long	1024
	.long	0
	.long	1024
	.long	0
	.long	0
	.long	2
	.quad	1048576
	.quad	13631488
	.quad	1048576
	.long	64
	.long	0
	.long	13
	.long	256
	.long	2048
	.long	0
	.long	256
	.long	0
	.long	0
	.long	4
	.quad	524288
	.quad	17825792
	.quad	524288
	.long	0
	.long	0
	.long	15
	.long	6144
	.long	1024
	.long	0
	.long	2048
	.long	0
	.long	0
	.long	2
	.quad	6291456
	.quad	22020096
	.quad	4194304
	.long	32
	.long	0
	.long	15
	.long	6144
	.long	1024
	.long	4096
	.long	2048
	.long	2048
	.long	0
	.long	2
	.quad	6291456
	.quad	22020096
	.quad	4194304
	.long	32
	.long	0
	.long	15
	.long	6144
	.long	1024
	.long	2048
	.long	2048
	.long	0
	.long	0
	.long	2
	.quad	6291456
	.quad	38797312
	.quad	2097152
	.long	32
	.long	0
	.long	16
	.long	1024
	.long	2048
	.long	0
	.long	1024
	.long	0
	.long	0
	.long	2
	.quad	2097152
	.quad	51380224
	.quad	2097152
	.long	128
	.long	0
	.long	20
	.long	2048
	.long	1024
	.long	0
	.long	2048
	.long	0
	.long	2
	.long	116
	.quad	2097152
	.quad	71303168
	.quad	2097152
	.long	32
	.long	0
	.long	22
	.long	1024
	.long	1024
	.long	0
	.long	1024
	.long	0
	.long	0
	.long	116
	.quad	1048576
	.quad	608174080
	.quad	1048576
	.long	64
	.long	0
	.long	24
	.long	1024
	.long	256
	.long	0
	.long	1024
	.long	0
	.long	0
	.long	4
	.quad	262144
	.quad	59768832
	.quad	262144
	.long	0
	.long	0
	.long	25
	.long	1024
	.long	1024
	.long	0
	.long	1024
	.long	0
	.long	0
	.long	4
	.quad	1048576
	.quad	61865984
	.quad	1048576
	.long	32
	.long	0
	.size	c_jobs, 1216

	.type	__hip_cuid_b50e1a6430de2f85,@object
